# v47 + P1 LayerNorm affine tail: gamma/beta quads of four column tiles kept in flight in free registers with counted waits (8 exposed load latencies -> 1)
# baseline (speedup 1.0000x reference)
.LBB0_132:
	s_or_b64 exec, exec, s[4:5]
	s_waitcnt lgkmcnt(1)
	v_and_b32_e32 v130, 0x78, v134
	v_add_u32_e32 v134, 0, v130
	v_add_u32_e32 v130, 0x20000, v134
	s_waitcnt lgkmcnt(0)
	s_barrier
	v_add_u32_e32 v132, 0x20200, v134
	ds_read_b64 v[130:131], v130
	ds_read_b64 v[132:133], v132
	v_add_u32_e32 v135, 0x20400, v134
	v_add_u32_e32 v136, 0x20600, v134
	v_add_u32_e32 v137, 0x20800, v134
	s_waitcnt lgkmcnt(1)
	v_pk_add_f32 v[130:131], v[130:131], 0 op_sel_hi:[1,0]
	v_add_u32_e32 v138, 0x20a00, v134
	s_waitcnt lgkmcnt(0)
	v_pk_add_f32 v[130:131], v[130:131], v[132:133]
	ds_read_b64 v[132:133], v135
	v_add_u32_e32 v139, 0x20c00, v134
	v_add_u32_e32 v140, 0x20e00, v134
	v_add_u32_e32 v142, 0x20a80, v134
	v_add_u32_e32 v143, 0x20c80, v134
	s_waitcnt lgkmcnt(0)
	v_pk_add_f32 v[130:131], v[130:131], v[132:133]
	ds_read_b64 v[132:133], v136
	v_add_u32_e32 v144, 0x20e80, v134
	v_add_u32_e32 v146, 0x20b00, v134
	v_add_u32_e32 v147, 0x20d00, v134
	v_add_u32_e32 v148, 0x20f00, v134
	s_waitcnt lgkmcnt(0)
	v_pk_add_f32 v[130:131], v[130:131], v[132:133]
	ds_read_b64 v[132:133], v137
	v_add_u32_e32 v137, 0x20880, v134
	v_add_u32_e32 v150, 0x20b80, v134
	v_add_u32_e32 v151, 0x20d80, v134
	s_load_dwordx4 s[12:15], s[0:1], 0x38
	s_waitcnt lgkmcnt(0)
	v_pk_add_f32 v[130:131], v[130:131], v[132:133]
	ds_read_b64 v[132:133], v138
	v_and_b32_e32 v145, 15, v221
	v_lshl_add_u32 v160, v145, 11, 0
	s_ashr_i32 s81, s80, 31
	s_mov_b32 s65, s23
	s_waitcnt lgkmcnt(0)
	v_pk_add_f32 v[130:131], v[130:131], v[132:133]
	ds_read_b64 v[132:133], v139
	s_mov_b32 s67, s23
	s_mov_b32 s69, s23
	s_mov_b32 s8, 3
	s_waitcnt lgkmcnt(0)
	v_pk_add_f32 v[130:131], v[130:131], v[132:133]
	ds_read_b64 v[132:133], v140
	s_waitcnt lgkmcnt(0)
	v_pk_add_f32 v[130:131], v[130:131], v[132:133]
	s_nop 0
	v_pk_mul_f32 v[138:139], v[130:131], s[76:77] op_sel_hi:[1,0]
	s_nop 0
	v_fma_f32 v130, -v138, v138, v139
	v_max_f32_e32 v130, 0, v130
	v_add_f32_e32 v130, 0x3727c5ac, v130
	v_cmp_gt_f32_e32 vcc, s7, v130
	v_mul_f32_e32 v131, 0x4f800000, v130
	v_pk_add_f32 v[126:127], v[126:127], v[138:139] op_sel_hi:[1,0] neg_lo:[0,1] neg_hi:[0,1]
	v_cndmask_b32_e32 v130, v130, v131, vcc
	v_sqrt_f32_e32 v131, v130
	v_pk_add_f32 v[128:129], v[128:129], v[138:139] op_sel_hi:[1,0] neg_lo:[0,1] neg_hi:[0,1]
	v_pk_add_f32 v[110:111], v[110:111], v[138:139] op_sel_hi:[1,0] neg_lo:[0,1] neg_hi:[0,1]
	v_pk_add_f32 v[112:113], v[112:113], v[138:139] op_sel_hi:[1,0] neg_lo:[0,1] neg_hi:[0,1]
	v_add_u32_e32 v132, -1, v131
	v_fma_f32 v133, -v132, v131, v130
	v_cmp_ge_f32_e64 s[4:5], 0, v133
	v_add_u32_e32 v133, 1, v131
	v_pk_add_f32 v[94:95], v[94:95], v[138:139] op_sel_hi:[1,0] neg_lo:[0,1] neg_hi:[0,1]
	v_cndmask_b32_e64 v132, v131, v132, s[4:5]
	v_fma_f32 v131, -v133, v131, v130
	v_cmp_lt_f32_e64 s[4:5], 0, v131
	v_pk_add_f32 v[96:97], v[96:97], v[138:139] op_sel_hi:[1,0] neg_lo:[0,1] neg_hi:[0,1]
	v_pk_add_f32 v[78:79], v[78:79], v[138:139] op_sel_hi:[1,0] neg_lo:[0,1] neg_hi:[0,1]
	v_cndmask_b32_e64 v131, v132, v133, s[4:5]
	v_mul_f32_e32 v132, 0x37800000, v131
	v_cndmask_b32_e32 v131, v131, v132, vcc
	v_cmp_class_f32_e32 vcc, v130, v218
	v_pk_add_f32 v[80:81], v[80:81], v[138:139] op_sel_hi:[1,0] neg_lo:[0,1] neg_hi:[0,1]
	v_pk_add_f32 v[62:63], v[62:63], v[138:139] op_sel_hi:[1,0] neg_lo:[0,1] neg_hi:[0,1]
	v_cndmask_b32_e32 v130, v131, v130, vcc
	v_div_scale_f32 v131, s[4:5], v130, v130, 1.0
	v_rcp_f32_e32 v132, v131
	v_pk_add_f32 v[64:65], v[64:65], v[138:139] op_sel_hi:[1,0] neg_lo:[0,1] neg_hi:[0,1]
	v_pk_add_f32 v[34:35], v[34:35], v[138:139] op_sel_hi:[1,0] neg_lo:[0,1] neg_hi:[0,1]
	v_pk_add_f32 v[36:37], v[36:37], v[138:139] op_sel_hi:[1,0] neg_lo:[0,1] neg_hi:[0,1]
	v_fma_f32 v133, -v131, v132, 1.0
	v_fmac_f32_e32 v132, v133, v132
	v_div_scale_f32 v133, vcc, 1.0, v130, 1.0
	v_mul_f32_e32 v135, v133, v132
	v_fma_f32 v136, -v131, v135, v133
	v_fmac_f32_e32 v135, v136, v132
	v_fma_f32 v131, -v131, v135, v133
	v_div_fmas_f32 v131, v131, v132, v135
	v_div_fixup_f32 v140, v131, v130, 1.0
	v_add_u32_e32 v130, 0x20080, v134
	v_add_u32_e32 v132, 0x20280, v134
	ds_read_b64 v[130:131], v130
	ds_read_b64 v[132:133], v132
	v_add_u32_e32 v135, 0x20480, v134
	v_add_u32_e32 v136, 0x20680, v134
	v_pk_mul_f32 v[126:127], v[126:127], v[140:141] op_sel_hi:[1,0]
	s_waitcnt lgkmcnt(1)
	v_pk_add_f32 v[130:131], v[130:131], 0 op_sel_hi:[1,0]
	v_pk_mul_f32 v[128:129], v[128:129], v[140:141] op_sel_hi:[1,0]
	s_waitcnt lgkmcnt(0)
	v_pk_add_f32 v[130:131], v[130:131], v[132:133]
	ds_read_b64 v[132:133], v135
	v_pk_mul_f32 v[110:111], v[110:111], v[140:141] op_sel_hi:[1,0]
	v_pk_mul_f32 v[112:113], v[112:113], v[140:141] op_sel_hi:[1,0]
	v_pk_mul_f32 v[94:95], v[94:95], v[140:141] op_sel_hi:[1,0]
	v_pk_mul_f32 v[96:97], v[96:97], v[140:141] op_sel_hi:[1,0]
	s_waitcnt lgkmcnt(0)
	v_pk_add_f32 v[130:131], v[130:131], v[132:133]
	ds_read_b64 v[132:133], v136
	v_pk_mul_f32 v[78:79], v[78:79], v[140:141] op_sel_hi:[1,0]
	v_pk_mul_f32 v[80:81], v[80:81], v[140:141] op_sel_hi:[1,0]
	v_pk_mul_f32 v[62:63], v[62:63], v[140:141] op_sel_hi:[1,0]
	v_pk_mul_f32 v[64:65], v[64:65], v[140:141] op_sel_hi:[1,0]
	s_waitcnt lgkmcnt(0)
	v_pk_add_f32 v[130:131], v[130:131], v[132:133]
	ds_read_b64 v[132:133], v137
	v_add_u32_e32 v137, 0x20900, v134
	v_pk_mul_f32 v[34:35], v[34:35], v[140:141] op_sel_hi:[1,0]
	v_pk_mul_f32 v[36:37], v[36:37], v[140:141] op_sel_hi:[1,0]
	v_pk_add_f32 v[14:15], v[14:15], v[138:139] op_sel_hi:[1,0] neg_lo:[0,1] neg_hi:[0,1]
	s_waitcnt lgkmcnt(0)
	v_pk_add_f32 v[130:131], v[130:131], v[132:133]
	ds_read_b64 v[132:133], v142
	v_pk_add_f32 v[16:17], v[16:17], v[138:139] op_sel_hi:[1,0] neg_lo:[0,1] neg_hi:[0,1]
	v_pk_mul_f32 v[14:15], v[14:15], v[140:141] op_sel_hi:[1,0]
	v_pk_mul_f32 v[16:17], v[16:17], v[140:141] op_sel_hi:[1,0]
	s_waitcnt lgkmcnt(0)
	v_pk_add_f32 v[130:131], v[130:131], v[132:133]
	ds_read_b64 v[132:133], v143
	s_waitcnt lgkmcnt(0)
	v_pk_add_f32 v[130:131], v[130:131], v[132:133]
	ds_read_b64 v[132:133], v144
	s_waitcnt lgkmcnt(0)
	v_pk_add_f32 v[130:131], v[130:131], v[132:133]
	s_nop 0
	v_pk_mul_f32 v[142:143], v[130:131], s[76:77] op_sel_hi:[1,0]
	s_nop 0
	v_fma_f32 v130, -v142, v142, v143
	v_max_f32_e32 v130, 0, v130
	v_add_f32_e32 v130, 0x3727c5ac, v130
	v_cmp_gt_f32_e32 vcc, s7, v130
	v_mul_f32_e32 v131, 0x4f800000, v130
	v_pk_add_f32 v[122:123], v[122:123], v[142:143] op_sel_hi:[1,0] neg_lo:[0,1] neg_hi:[0,1]
	v_cndmask_b32_e32 v130, v130, v131, vcc
	v_sqrt_f32_e32 v131, v130
	v_pk_add_f32 v[124:125], v[124:125], v[142:143] op_sel_hi:[1,0] neg_lo:[0,1] neg_hi:[0,1]
	v_pk_add_f32 v[106:107], v[106:107], v[142:143] op_sel_hi:[1,0] neg_lo:[0,1] neg_hi:[0,1]
	v_pk_add_f32 v[108:109], v[108:109], v[142:143] op_sel_hi:[1,0] neg_lo:[0,1] neg_hi:[0,1]
	v_add_u32_e32 v132, -1, v131
	v_fma_f32 v133, -v132, v131, v130
	v_cmp_ge_f32_e64 s[4:5], 0, v133
	v_add_u32_e32 v133, 1, v131
	v_pk_add_f32 v[90:91], v[90:91], v[142:143] op_sel_hi:[1,0] neg_lo:[0,1] neg_hi:[0,1]
	v_cndmask_b32_e64 v132, v131, v132, s[4:5]
	v_fma_f32 v131, -v133, v131, v130
	v_cmp_lt_f32_e64 s[4:5], 0, v131
	v_pk_add_f32 v[92:93], v[92:93], v[142:143] op_sel_hi:[1,0] neg_lo:[0,1] neg_hi:[0,1]
	v_pk_add_f32 v[74:75], v[74:75], v[142:143] op_sel_hi:[1,0] neg_lo:[0,1] neg_hi:[0,1]
	v_cndmask_b32_e64 v131, v132, v133, s[4:5]
	v_mul_f32_e32 v132, 0x37800000, v131
	v_cndmask_b32_e32 v131, v131, v132, vcc
	v_cmp_class_f32_e32 vcc, v130, v218
	v_pk_add_f32 v[76:77], v[76:77], v[142:143] op_sel_hi:[1,0] neg_lo:[0,1] neg_hi:[0,1]
	v_pk_add_f32 v[54:55], v[54:55], v[142:143] op_sel_hi:[1,0] neg_lo:[0,1] neg_hi:[0,1]
	v_cndmask_b32_e32 v130, v131, v130, vcc
	v_div_scale_f32 v131, s[4:5], v130, v130, 1.0
	v_rcp_f32_e32 v132, v131
	v_pk_add_f32 v[56:57], v[56:57], v[142:143] op_sel_hi:[1,0] neg_lo:[0,1] neg_hi:[0,1]
	v_pk_add_f32 v[50:51], v[50:51], v[142:143] op_sel_hi:[1,0] neg_lo:[0,1] neg_hi:[0,1]
	v_pk_add_f32 v[52:53], v[52:53], v[142:143] op_sel_hi:[1,0] neg_lo:[0,1] neg_hi:[0,1]
	v_fma_f32 v133, -v131, v132, 1.0
	v_fmac_f32_e32 v132, v133, v132
	v_div_scale_f32 v133, vcc, 1.0, v130, 1.0
	v_mul_f32_e32 v135, v133, v132
	v_fma_f32 v136, -v131, v135, v133
	v_fmac_f32_e32 v135, v136, v132
	v_fma_f32 v131, -v131, v135, v133
	v_div_fmas_f32 v131, v131, v132, v135
	v_div_fixup_f32 v144, v131, v130, 1.0
	v_add_u32_e32 v130, 0x20100, v134
	v_add_u32_e32 v132, 0x20300, v134
	ds_read_b64 v[130:131], v130
	ds_read_b64 v[132:133], v132
	v_add_u32_e32 v135, 0x20500, v134
	v_add_u32_e32 v136, 0x20700, v134
	v_pk_mul_f32 v[122:123], v[122:123], v[144:145] op_sel_hi:[1,0]
	s_waitcnt lgkmcnt(1)
	v_pk_add_f32 v[130:131], v[130:131], 0 op_sel_hi:[1,0]
	v_pk_mul_f32 v[124:125], v[124:125], v[144:145] op_sel_hi:[1,0]
	s_waitcnt lgkmcnt(0)
	v_pk_add_f32 v[130:131], v[130:131], v[132:133]
	ds_read_b64 v[132:133], v135
	v_pk_mul_f32 v[106:107], v[106:107], v[144:145] op_sel_hi:[1,0]
	v_pk_mul_f32 v[108:109], v[108:109], v[144:145] op_sel_hi:[1,0]
	v_pk_mul_f32 v[90:91], v[90:91], v[144:145] op_sel_hi:[1,0]
	v_pk_mul_f32 v[92:93], v[92:93], v[144:145] op_sel_hi:[1,0]
	s_waitcnt lgkmcnt(0)
	v_pk_add_f32 v[130:131], v[130:131], v[132:133]
	ds_read_b64 v[132:133], v136
	v_pk_mul_f32 v[74:75], v[74:75], v[144:145] op_sel_hi:[1,0]
	v_pk_mul_f32 v[76:77], v[76:77], v[144:145] op_sel_hi:[1,0]
	v_pk_mul_f32 v[54:55], v[54:55], v[144:145] op_sel_hi:[1,0]
	v_pk_mul_f32 v[56:57], v[56:57], v[144:145] op_sel_hi:[1,0]
	s_waitcnt lgkmcnt(0)
	v_pk_add_f32 v[130:131], v[130:131], v[132:133]
	ds_read_b64 v[132:133], v137
	v_add_u32_e32 v137, 0x20980, v134
	v_pk_mul_f32 v[50:51], v[50:51], v[144:145] op_sel_hi:[1,0]
	v_pk_mul_f32 v[52:53], v[52:53], v[144:145] op_sel_hi:[1,0]
	v_pk_add_f32 v[30:31], v[30:31], v[142:143] op_sel_hi:[1,0] neg_lo:[0,1] neg_hi:[0,1]
	s_waitcnt lgkmcnt(0)
	v_pk_add_f32 v[130:131], v[130:131], v[132:133]
	ds_read_b64 v[132:133], v146
	v_pk_add_f32 v[32:33], v[32:33], v[142:143] op_sel_hi:[1,0] neg_lo:[0,1] neg_hi:[0,1]
	v_pk_mul_f32 v[30:31], v[30:31], v[144:145] op_sel_hi:[1,0]
	v_pk_mul_f32 v[32:33], v[32:33], v[144:145] op_sel_hi:[1,0]
	v_pk_add_f32 v[10:11], v[10:11], v[142:143] op_sel_hi:[1,0] neg_lo:[0,1] neg_hi:[0,1]
	s_waitcnt lgkmcnt(0)
	v_pk_add_f32 v[130:131], v[130:131], v[132:133]
	ds_read_b64 v[132:133], v147
	v_pk_add_f32 v[12:13], v[12:13], v[142:143] op_sel_hi:[1,0] neg_lo:[0,1] neg_hi:[0,1]
	v_pk_mul_f32 v[10:11], v[10:11], v[144:145] op_sel_hi:[1,0]
	v_pk_mul_f32 v[12:13], v[12:13], v[144:145] op_sel_hi:[1,0]
	s_waitcnt lgkmcnt(0)
	v_pk_add_f32 v[130:131], v[130:131], v[132:133]
	ds_read_b64 v[132:133], v148
	s_waitcnt lgkmcnt(0)
	v_pk_add_f32 v[130:131], v[130:131], v[132:133]
	s_nop 0
	v_pk_mul_f32 v[146:147], v[130:131], s[76:77] op_sel_hi:[1,0]
	s_nop 0
	v_fma_f32 v130, -v146, v146, v147
	v_max_f32_e32 v130, 0, v130
	v_add_f32_e32 v130, 0x3727c5ac, v130
	v_cmp_gt_f32_e32 vcc, s7, v130
	v_mul_f32_e32 v131, 0x4f800000, v130
	v_pk_add_f32 v[118:119], v[118:119], v[146:147] op_sel_hi:[1,0] neg_lo:[0,1] neg_hi:[0,1]
	v_cndmask_b32_e32 v130, v130, v131, vcc
	v_sqrt_f32_e32 v131, v130
	v_pk_add_f32 v[120:121], v[120:121], v[146:147] op_sel_hi:[1,0] neg_lo:[0,1] neg_hi:[0,1]
	v_pk_add_f32 v[102:103], v[102:103], v[146:147] op_sel_hi:[1,0] neg_lo:[0,1] neg_hi:[0,1]
	v_pk_add_f32 v[104:105], v[104:105], v[146:147] op_sel_hi:[1,0] neg_lo:[0,1] neg_hi:[0,1]
	v_add_u32_e32 v132, -1, v131
	v_fma_f32 v133, -v132, v131, v130
	v_cmp_ge_f32_e64 s[4:5], 0, v133
	v_add_u32_e32 v133, 1, v131
	v_pk_add_f32 v[86:87], v[86:87], v[146:147] op_sel_hi:[1,0] neg_lo:[0,1] neg_hi:[0,1]
	v_cndmask_b32_e64 v132, v131, v132, s[4:5]
	v_fma_f32 v131, -v133, v131, v130
	v_cmp_lt_f32_e64 s[4:5], 0, v131
	v_pk_add_f32 v[88:89], v[88:89], v[146:147] op_sel_hi:[1,0] neg_lo:[0,1] neg_hi:[0,1]
	v_pk_add_f32 v[70:71], v[70:71], v[146:147] op_sel_hi:[1,0] neg_lo:[0,1] neg_hi:[0,1]
	v_cndmask_b32_e64 v131, v132, v133, s[4:5]
	v_mul_f32_e32 v132, 0x37800000, v131
	v_cndmask_b32_e32 v131, v131, v132, vcc
	v_cmp_class_f32_e32 vcc, v130, v218
	v_pk_add_f32 v[72:73], v[72:73], v[146:147] op_sel_hi:[1,0] neg_lo:[0,1] neg_hi:[0,1]
	v_pk_add_f32 v[46:47], v[46:47], v[146:147] op_sel_hi:[1,0] neg_lo:[0,1] neg_hi:[0,1]
	v_cndmask_b32_e32 v130, v131, v130, vcc
	v_div_scale_f32 v131, s[4:5], v130, v130, 1.0
	v_rcp_f32_e32 v132, v131
	v_pk_add_f32 v[48:49], v[48:49], v[146:147] op_sel_hi:[1,0] neg_lo:[0,1] neg_hi:[0,1]
	v_pk_add_f32 v[42:43], v[42:43], v[146:147] op_sel_hi:[1,0] neg_lo:[0,1] neg_hi:[0,1]
	v_pk_add_f32 v[44:45], v[44:45], v[146:147] op_sel_hi:[1,0] neg_lo:[0,1] neg_hi:[0,1]
	v_fma_f32 v133, -v131, v132, 1.0
	v_fmac_f32_e32 v132, v133, v132
	v_div_scale_f32 v133, vcc, 1.0, v130, 1.0
	v_mul_f32_e32 v135, v133, v132
	v_fma_f32 v136, -v131, v135, v133
	v_fmac_f32_e32 v135, v136, v132
	v_fma_f32 v131, -v131, v135, v133
	v_div_fmas_f32 v131, v131, v132, v135
	v_div_fixup_f32 v148, v131, v130, 1.0
	v_add_u32_e32 v130, 0x20180, v134
	v_add_u32_e32 v132, 0x20380, v134
	ds_read_b64 v[130:131], v130
	ds_read_b64 v[132:133], v132
	v_add_u32_e32 v135, 0x20580, v134
	v_add_u32_e32 v136, 0x20780, v134
	v_add_u32_e32 v134, 0x20f80, v134
	s_waitcnt lgkmcnt(1)
	v_pk_add_f32 v[130:131], v[130:131], 0 op_sel_hi:[1,0]
	v_pk_mul_f32 v[118:119], v[118:119], v[148:149] op_sel_hi:[1,0]
	s_waitcnt lgkmcnt(0)
	v_pk_add_f32 v[130:131], v[130:131], v[132:133]
	ds_read_b64 v[132:133], v135
	v_pk_mul_f32 v[120:121], v[120:121], v[148:149] op_sel_hi:[1,0]
	v_pk_mul_f32 v[102:103], v[102:103], v[148:149] op_sel_hi:[1,0]
	v_pk_mul_f32 v[104:105], v[104:105], v[148:149] op_sel_hi:[1,0]
	v_pk_mul_f32 v[86:87], v[86:87], v[148:149] op_sel_hi:[1,0]
	s_waitcnt lgkmcnt(0)
	v_pk_add_f32 v[130:131], v[130:131], v[132:133]
	ds_read_b64 v[132:133], v136
	v_pk_mul_f32 v[88:89], v[88:89], v[148:149] op_sel_hi:[1,0]
	v_pk_mul_f32 v[70:71], v[70:71], v[148:149] op_sel_hi:[1,0]
	v_pk_mul_f32 v[72:73], v[72:73], v[148:149] op_sel_hi:[1,0]
	v_pk_mul_f32 v[46:47], v[46:47], v[148:149] op_sel_hi:[1,0]
	s_waitcnt lgkmcnt(0)
	v_pk_add_f32 v[130:131], v[130:131], v[132:133]
	ds_read_b64 v[132:133], v137
	v_pk_mul_f32 v[48:49], v[48:49], v[148:149] op_sel_hi:[1,0]
	v_pk_mul_f32 v[42:43], v[42:43], v[148:149] op_sel_hi:[1,0]
	v_pk_mul_f32 v[44:45], v[44:45], v[148:149] op_sel_hi:[1,0]
	v_pk_add_f32 v[26:27], v[26:27], v[146:147] op_sel_hi:[1,0] neg_lo:[0,1] neg_hi:[0,1]
	s_waitcnt lgkmcnt(0)
	v_pk_add_f32 v[130:131], v[130:131], v[132:133]
	ds_read_b64 v[132:133], v150
	v_pk_add_f32 v[28:29], v[28:29], v[146:147] op_sel_hi:[1,0] neg_lo:[0,1] neg_hi:[0,1]
	v_pk_mul_f32 v[26:27], v[26:27], v[148:149] op_sel_hi:[1,0]
	v_pk_mul_f32 v[28:29], v[28:29], v[148:149] op_sel_hi:[1,0]
	v_pk_add_f32 v[6:7], v[6:7], v[146:147] op_sel_hi:[1,0] neg_lo:[0,1] neg_hi:[0,1]
	s_waitcnt lgkmcnt(0)
	v_pk_add_f32 v[130:131], v[130:131], v[132:133]
	ds_read_b64 v[132:133], v151
	v_pk_add_f32 v[8:9], v[8:9], v[146:147] op_sel_hi:[1,0] neg_lo:[0,1] neg_hi:[0,1]
	v_pk_mul_f32 v[6:7], v[6:7], v[148:149] op_sel_hi:[1,0]
	v_pk_mul_f32 v[8:9], v[8:9], v[148:149] op_sel_hi:[1,0]
	s_waitcnt lgkmcnt(0)
	v_pk_add_f32 v[130:131], v[130:131], v[132:133]
	ds_read_b64 v[132:133], v134
	s_waitcnt lgkmcnt(0)
	v_pk_add_f32 v[130:131], v[130:131], v[132:133]
	s_nop 0
	v_pk_mul_f32 v[150:151], v[130:131], s[76:77] op_sel_hi:[1,0]
	s_nop 0
	v_fma_f32 v130, -v150, v150, v151
	v_max_f32_e32 v130, 0, v130
	v_add_f32_e32 v130, 0x3727c5ac, v130
	v_cmp_gt_f32_e32 vcc, s7, v130
	v_mul_f32_e32 v131, 0x4f800000, v130
	v_pk_add_f32 v[114:115], v[114:115], v[150:151] op_sel_hi:[1,0] neg_lo:[0,1] neg_hi:[0,1]
	v_cndmask_b32_e32 v130, v130, v131, vcc
	v_sqrt_f32_e32 v131, v130
	v_pk_add_f32 v[116:117], v[116:117], v[150:151] op_sel_hi:[1,0] neg_lo:[0,1] neg_hi:[0,1]
	v_pk_add_f32 v[98:99], v[98:99], v[150:151] op_sel_hi:[1,0] neg_lo:[0,1] neg_hi:[0,1]
	v_pk_add_f32 v[100:101], v[100:101], v[150:151] op_sel_hi:[1,0] neg_lo:[0,1] neg_hi:[0,1]
	v_add_u32_e32 v132, -1, v131
	v_fma_f32 v133, -v132, v131, v130
	v_cmp_ge_f32_e64 s[4:5], 0, v133
	v_add_u32_e32 v133, 1, v131
	v_pk_add_f32 v[82:83], v[82:83], v[150:151] op_sel_hi:[1,0] neg_lo:[0,1] neg_hi:[0,1]
	v_cndmask_b32_e64 v132, v131, v132, s[4:5]
	v_fma_f32 v131, -v133, v131, v130
	v_cmp_lt_f32_e64 s[4:5], 0, v131
	v_pk_add_f32 v[84:85], v[84:85], v[150:151] op_sel_hi:[1,0] neg_lo:[0,1] neg_hi:[0,1]
	v_pk_add_f32 v[66:67], v[66:67], v[150:151] op_sel_hi:[1,0] neg_lo:[0,1] neg_hi:[0,1]
	v_cndmask_b32_e64 v131, v132, v133, s[4:5]
	v_mul_f32_e32 v132, 0x37800000, v131
	v_cndmask_b32_e32 v131, v131, v132, vcc
	v_cmp_class_f32_e32 vcc, v130, v218
	v_pk_add_f32 v[68:69], v[68:69], v[150:151] op_sel_hi:[1,0] neg_lo:[0,1] neg_hi:[0,1]
	v_pk_add_f32 v[38:39], v[38:39], v[150:151] op_sel_hi:[1,0] neg_lo:[0,1] neg_hi:[0,1]
	v_cndmask_b32_e32 v130, v131, v130, vcc
	v_div_scale_f32 v131, s[4:5], v130, v130, 1.0
	v_rcp_f32_e32 v132, v131
	v_pk_add_f32 v[40:41], v[40:41], v[150:151] op_sel_hi:[1,0] neg_lo:[0,1] neg_hi:[0,1]
	v_pk_add_f32 v[22:23], v[22:23], v[150:151] op_sel_hi:[1,0] neg_lo:[0,1] neg_hi:[0,1]
	v_pk_add_f32 v[24:25], v[24:25], v[150:151] op_sel_hi:[1,0] neg_lo:[0,1] neg_hi:[0,1]
	v_fma_f32 v133, -v131, v132, 1.0
	v_fmac_f32_e32 v132, v133, v132
	v_div_scale_f32 v133, vcc, 1.0, v130, 1.0
	v_mul_f32_e32 v134, v133, v132
	v_fma_f32 v135, -v131, v134, v133
	v_fmac_f32_e32 v134, v135, v132
	v_fma_f32 v131, -v131, v134, v133
	v_div_fmas_f32 v131, v131, v132, v134
	v_div_fixup_f32 v152, v131, v130, 1.0
	v_lshrrev_b32_e32 v130, 2, v221
	v_and_or_b32 v158, v130, 12, s29
	v_ashrrev_i32_e32 v159, 31, v158
	v_lshlrev_b64 v[130:131], 2, v[158:159]
	v_lshl_add_u64 v[156:157], s[12:13], 0, v[130:131]
	v_lshl_add_u64 v[154:155], s[14:15], 0, v[130:131]
	v_lshrrev_b32_e32 v130, 3, v158
	v_bitop3_b32 v130, v130, v221, 15 bitop3:0x78
	v_lshrrev_b32_e32 v131, 1, v221
	v_lshlrev_b32_e32 v130, 4, v130
	v_and_b32_e32 v159, 8, v131
	v_add3_u32 v161, v160, v130, v159
	global_load_dwordx4 v[226:229], v[156:157], off
	global_load_dwordx4 v[230:233], v[154:155], off
	global_load_dwordx4 v[234:237], v[156:157], off offset:64
	global_load_dwordx4 v[238:241], v[154:155], off offset:64
	global_load_dwordx4 v[242:245], v[156:157], off offset:128
	global_load_dwordx4 v[246:249], v[154:155], off offset:128
	global_load_dwordx4 v[250:253], v[156:157], off offset:192
	global_load_dwordx4 v[204:207], v[154:155], off offset:192
	v_pk_mul_f32 v[114:115], v[114:115], v[152:153] op_sel_hi:[1,0]
	v_pk_mul_f32 v[116:117], v[116:117], v[152:153] op_sel_hi:[1,0]
	v_pk_mul_f32 v[98:99], v[98:99], v[152:153] op_sel_hi:[1,0]
	v_pk_mul_f32 v[100:101], v[100:101], v[152:153] op_sel_hi:[1,0]
	v_pk_mul_f32 v[82:83], v[82:83], v[152:153] op_sel_hi:[1,0]
	v_pk_mul_f32 v[84:85], v[84:85], v[152:153] op_sel_hi:[1,0]
	v_pk_mul_f32 v[66:67], v[66:67], v[152:153] op_sel_hi:[1,0]
	v_pk_mul_f32 v[68:69], v[68:69], v[152:153] op_sel_hi:[1,0]
	v_pk_mul_f32 v[38:39], v[38:39], v[152:153] op_sel_hi:[1,0]
	v_pk_mul_f32 v[40:41], v[40:41], v[152:153] op_sel_hi:[1,0]
	v_pk_mul_f32 v[22:23], v[22:23], v[152:153] op_sel_hi:[1,0]
	v_pk_mul_f32 v[24:25], v[24:25], v[152:153] op_sel_hi:[1,0]
	v_pk_add_f32 v[18:19], v[18:19], v[150:151] op_sel_hi:[1,0] neg_lo:[0,1] neg_hi:[0,1]
	v_pk_add_f32 v[20:21], v[20:21], v[150:151] op_sel_hi:[1,0] neg_lo:[0,1] neg_hi:[0,1]
	v_pk_mul_f32 v[18:19], v[18:19], v[152:153] op_sel_hi:[1,0]
	v_pk_mul_f32 v[20:21], v[20:21], v[152:153] op_sel_hi:[1,0]
	v_pk_add_f32 v[2:3], v[2:3], v[150:151] op_sel_hi:[1,0] neg_lo:[0,1] neg_hi:[0,1]
	v_pk_add_f32 v[4:5], v[4:5], v[150:151] op_sel_hi:[1,0] neg_lo:[0,1] neg_hi:[0,1]
	v_pk_mul_f32 v[2:3], v[2:3], v[152:153] op_sel_hi:[1,0]
	v_pk_mul_f32 v[4:5], v[4:5], v[152:153] op_sel_hi:[1,0]
	s_lshl_b64 s[4:5], s[80:81], 11
	s_waitcnt vmcnt(6)
	v_pk_fma_f32 v[114:115], v[226:227], v[114:115], v[230:231]
	v_pk_fma_f32 v[116:117], v[228:229], v[116:117], v[232:233]
	v_cvt_pk_bf16_f32 v114, v114, v115
	v_cvt_pk_bf16_f32 v115, v116, v117
	v_add_u32_e32 v116, 0x18000, v161
	v_pk_fma_f32 v[126:127], v[126:127], v[226:227], v[230:231]
	v_pk_fma_f32 v[128:129], v[128:129], v[228:229], v[232:233]
	v_pk_fma_f32 v[122:123], v[122:123], v[226:227], v[230:231]
	v_pk_fma_f32 v[124:125], v[124:125], v[228:229], v[232:233]
	v_pk_fma_f32 v[118:119], v[118:119], v[226:227], v[230:231]
	v_pk_fma_f32 v[120:121], v[120:121], v[228:229], v[232:233]
	global_load_dwordx4 v[226:229], v[156:157], off offset:256
	global_load_dwordx4 v[230:233], v[154:155], off offset:256
	ds_write_b64 v116, v[114:115]
	v_or_b32_e32 v114, 16, v158
	v_cvt_pk_bf16_f32 v126, v126, v127
	v_cvt_pk_bf16_f32 v127, v128, v129
	v_cvt_pk_bf16_f32 v122, v122, v123
	v_cvt_pk_bf16_f32 v123, v124, v125
	v_cvt_pk_bf16_f32 v118, v118, v119
	v_cvt_pk_bf16_f32 v119, v120, v121
	v_add_u32_e32 v120, 0x10000, v161
	v_lshrrev_b32_e32 v114, 3, v114
	ds_write2st64_b64 v161, v[126:127], v[122:123] offset1:64
	ds_write_b64 v120, v[118:119]
	v_bitop3_b32 v114, v114, v221, 15 bitop3:0x78
	v_lshlrev_b32_e32 v114, 4, v114
	v_add3_u32 v122, v160, v114, v159
	s_waitcnt vmcnt(6)
	v_pk_fma_f32 v[98:99], v[98:99], v[234:235], v[238:239]
	v_pk_fma_f32 v[100:101], v[100:101], v[236:237], v[240:241]
	v_cvt_pk_bf16_f32 v98, v98, v99
	v_cvt_pk_bf16_f32 v99, v100, v101
	v_add_u32_e32 v100, 0x18000, v122
	v_pk_fma_f32 v[110:111], v[110:111], v[234:235], v[238:239]
	v_pk_fma_f32 v[112:113], v[112:113], v[236:237], v[240:241]
	v_pk_fma_f32 v[106:107], v[106:107], v[234:235], v[238:239]
	v_pk_fma_f32 v[108:109], v[108:109], v[236:237], v[240:241]
	v_pk_fma_f32 v[102:103], v[102:103], v[234:235], v[238:239]
	v_pk_fma_f32 v[104:105], v[104:105], v[236:237], v[240:241]
	global_load_dwordx4 v[234:237], v[156:157], off offset:320
	global_load_dwordx4 v[238:241], v[154:155], off offset:320
	ds_write_b64 v100, v[98:99]
	v_or_b32_e32 v98, 32, v158
	v_cvt_pk_bf16_f32 v110, v110, v111
	v_cvt_pk_bf16_f32 v111, v112, v113
	v_cvt_pk_bf16_f32 v106, v106, v107
	v_cvt_pk_bf16_f32 v107, v108, v109
	v_cvt_pk_bf16_f32 v102, v102, v103
	v_cvt_pk_bf16_f32 v103, v104, v105
	v_add_u32_e32 v104, 0x10000, v122
	v_lshrrev_b32_e32 v98, 3, v98
	ds_write2st64_b64 v122, v[110:111], v[106:107] offset1:64
	ds_write_b64 v104, v[102:103]
	v_bitop3_b32 v98, v98, v221, 15 bitop3:0x78
	v_lshlrev_b32_e32 v98, 4, v98
	v_add3_u32 v106, v160, v98, v159
	s_waitcnt vmcnt(6)
	v_pk_fma_f32 v[82:83], v[82:83], v[242:243], v[246:247]
	v_pk_fma_f32 v[84:85], v[84:85], v[244:245], v[248:249]
	v_cvt_pk_bf16_f32 v82, v82, v83
	v_cvt_pk_bf16_f32 v83, v84, v85
	v_add_u32_e32 v84, 0x18000, v106
	v_pk_fma_f32 v[94:95], v[94:95], v[242:243], v[246:247]
	v_pk_fma_f32 v[96:97], v[96:97], v[244:245], v[248:249]
	v_pk_fma_f32 v[90:91], v[90:91], v[242:243], v[246:247]
	v_pk_fma_f32 v[92:93], v[92:93], v[244:245], v[248:249]
	v_pk_fma_f32 v[86:87], v[86:87], v[242:243], v[246:247]
	v_pk_fma_f32 v[88:89], v[88:89], v[244:245], v[248:249]
	global_load_dwordx4 v[242:245], v[156:157], off offset:384
	global_load_dwordx4 v[246:249], v[154:155], off offset:384
	ds_write_b64 v84, v[82:83]
	v_or_b32_e32 v82, 48, v158
	v_cvt_pk_bf16_f32 v94, v94, v95
	v_cvt_pk_bf16_f32 v95, v96, v97
	v_cvt_pk_bf16_f32 v90, v90, v91
	v_cvt_pk_bf16_f32 v91, v92, v93
	v_cvt_pk_bf16_f32 v86, v86, v87
	v_cvt_pk_bf16_f32 v87, v88, v89
	v_add_u32_e32 v88, 0x10000, v106
	v_lshrrev_b32_e32 v82, 3, v82
	ds_write2st64_b64 v106, v[94:95], v[90:91] offset1:64
	ds_write_b64 v88, v[86:87]
	v_bitop3_b32 v82, v82, v221, 15 bitop3:0x78
	v_lshlrev_b32_e32 v82, 4, v82
	v_add3_u32 v90, v160, v82, v159
	v_lshrrev_b32_e32 v100, 4, v141
	s_waitcnt vmcnt(6)
	v_pk_fma_f32 v[66:67], v[66:67], v[250:251], v[204:205]
	v_pk_fma_f32 v[68:69], v[68:69], v[252:253], v[206:207]
	v_cvt_pk_bf16_f32 v66, v66, v67
	v_cvt_pk_bf16_f32 v67, v68, v69
	v_add_u32_e32 v68, 0x18000, v90
	v_pk_fma_f32 v[78:79], v[78:79], v[250:251], v[204:205]
	v_pk_fma_f32 v[80:81], v[80:81], v[252:253], v[206:207]
	v_pk_fma_f32 v[74:75], v[74:75], v[250:251], v[204:205]
	v_pk_fma_f32 v[76:77], v[76:77], v[252:253], v[206:207]
	v_pk_fma_f32 v[70:71], v[70:71], v[250:251], v[204:205]
	v_pk_fma_f32 v[72:73], v[72:73], v[252:253], v[206:207]
	global_load_dwordx4 v[250:253], v[156:157], off offset:448
	global_load_dwordx4 v[204:207], v[154:155], off offset:448
	ds_write_b64 v68, v[66:67]
	v_or_b32_e32 v66, 64, v158
	v_cvt_pk_bf16_f32 v78, v78, v79
	v_cvt_pk_bf16_f32 v79, v80, v81
	v_cvt_pk_bf16_f32 v74, v74, v75
	v_cvt_pk_bf16_f32 v75, v76, v77
	v_cvt_pk_bf16_f32 v70, v70, v71
	v_cvt_pk_bf16_f32 v71, v72, v73
	v_add_u32_e32 v72, 0x10000, v90
	v_lshrrev_b32_e32 v66, 3, v66
	ds_write2st64_b64 v90, v[78:79], v[74:75] offset1:64
	ds_write_b64 v72, v[70:71]
	v_bitop3_b32 v66, v66, v221, 15 bitop3:0x78
	v_lshlrev_b32_e32 v66, 4, v66
	v_add3_u32 v74, v160, v66, v159
	s_waitcnt vmcnt(6)
	v_pk_fma_f32 v[38:39], v[38:39], v[226:227], v[230:231]
	v_pk_fma_f32 v[40:41], v[40:41], v[228:229], v[232:233]
	v_cvt_pk_bf16_f32 v38, v38, v39
	v_cvt_pk_bf16_f32 v39, v40, v41
	v_add_u32_e32 v40, 0x18000, v74
	v_pk_fma_f32 v[62:63], v[62:63], v[226:227], v[230:231]
	v_pk_fma_f32 v[64:65], v[64:65], v[228:229], v[232:233]
	v_pk_fma_f32 v[54:55], v[54:55], v[226:227], v[230:231]
	v_pk_fma_f32 v[56:57], v[56:57], v[228:229], v[232:233]
	v_pk_fma_f32 v[46:47], v[46:47], v[226:227], v[230:231]
	v_pk_fma_f32 v[48:49], v[48:49], v[228:229], v[232:233]
	ds_write_b64 v40, v[38:39]
	v_or_b32_e32 v38, 0x50, v158
	v_cvt_pk_bf16_f32 v62, v62, v63
	v_cvt_pk_bf16_f32 v63, v64, v65
	v_cvt_pk_bf16_f32 v54, v54, v55
	v_cvt_pk_bf16_f32 v55, v56, v57
	v_cvt_pk_bf16_f32 v46, v46, v47
	v_cvt_pk_bf16_f32 v47, v48, v49
	v_add_u32_e32 v48, 0x10000, v74
	v_lshrrev_b32_e32 v38, 3, v38
	ds_write2st64_b64 v74, v[62:63], v[54:55] offset1:64
	ds_write_b64 v48, v[46:47]
	v_bitop3_b32 v38, v38, v221, 15 bitop3:0x78
	v_lshlrev_b32_e32 v38, 4, v38
	v_add3_u32 v62, v160, v38, v159
	v_pk_add_f32 v[54:55], v[58:59], v[138:139] op_sel_hi:[1,0] neg_lo:[0,1] neg_hi:[0,1]
	v_pk_add_f32 v[56:57], v[60:61], v[138:139] op_sel_hi:[1,0] neg_lo:[0,1] neg_hi:[0,1]
	v_pk_mul_f32 v[54:55], v[54:55], v[140:141] op_sel_hi:[1,0]
	v_pk_mul_f32 v[56:57], v[56:57], v[140:141] op_sel_hi:[1,0]
	s_waitcnt vmcnt(4)
	v_pk_fma_f32 v[22:23], v[22:23], v[234:235], v[238:239]
	v_pk_fma_f32 v[24:25], v[24:25], v[236:237], v[240:241]
	v_cvt_pk_bf16_f32 v22, v22, v23
	v_cvt_pk_bf16_f32 v23, v24, v25
	v_add_u32_e32 v24, 0x18000, v62
	v_pk_fma_f32 v[54:55], v[54:55], v[234:235], v[238:239]
	v_pk_fma_f32 v[56:57], v[56:57], v[236:237], v[240:241]
	v_pk_fma_f32 v[50:51], v[50:51], v[234:235], v[238:239]
	v_pk_fma_f32 v[52:53], v[52:53], v[236:237], v[240:241]
	v_pk_fma_f32 v[42:43], v[42:43], v[234:235], v[238:239]
	v_pk_fma_f32 v[44:45], v[44:45], v[236:237], v[240:241]
	ds_write_b64 v24, v[22:23]
	v_or_b32_e32 v22, 0x60, v158
	v_cvt_pk_bf16_f32 v54, v54, v55
	v_cvt_pk_bf16_f32 v55, v56, v57
	v_cvt_pk_bf16_f32 v50, v50, v51
	v_cvt_pk_bf16_f32 v51, v52, v53
	v_cvt_pk_bf16_f32 v42, v42, v43
	v_cvt_pk_bf16_f32 v43, v44, v45
	v_add_u32_e32 v44, 0x10000, v62
	v_lshrrev_b32_e32 v22, 3, v22
	ds_write2st64_b64 v62, v[54:55], v[50:51] offset1:64
	ds_write_b64 v44, v[42:43]
	v_bitop3_b32 v22, v22, v221, 15 bitop3:0x78
	v_lshlrev_b32_e32 v22, 4, v22
	v_add3_u32 v42, v160, v22, v159
	s_waitcnt vmcnt(2)
	v_pk_fma_f32 v[18:19], v[18:19], v[242:243], v[246:247]
	v_pk_fma_f32 v[20:21], v[20:21], v[244:245], v[248:249]
	v_cvt_pk_bf16_f32 v18, v18, v19
	v_cvt_pk_bf16_f32 v19, v20, v21
	v_add_u32_e32 v20, 0x18000, v42
	v_pk_fma_f32 v[34:35], v[34:35], v[242:243], v[246:247]
	v_pk_fma_f32 v[36:37], v[36:37], v[244:245], v[248:249]
	v_pk_fma_f32 v[30:31], v[30:31], v[242:243], v[246:247]
	v_pk_fma_f32 v[32:33], v[32:33], v[244:245], v[248:249]
	v_pk_fma_f32 v[26:27], v[26:27], v[242:243], v[246:247]
	v_pk_fma_f32 v[28:29], v[28:29], v[244:245], v[248:249]
	ds_write_b64 v20, v[18:19]
	v_or_b32_e32 v18, 0x70, v158
	v_cvt_pk_bf16_f32 v34, v34, v35
	v_cvt_pk_bf16_f32 v35, v36, v37
	v_cvt_pk_bf16_f32 v30, v30, v31
	v_cvt_pk_bf16_f32 v31, v32, v33
	v_cvt_pk_bf16_f32 v26, v26, v27
	v_cvt_pk_bf16_f32 v27, v28, v29
	v_add_u32_e32 v28, 0x10000, v42
	v_lshrrev_b32_e32 v18, 3, v18
	ds_write2st64_b64 v42, v[34:35], v[30:31] offset1:64
	ds_write_b64 v28, v[26:27]
	v_bitop3_b32 v18, v18, v221, 15 bitop3:0x78
	v_lshlrev_b32_e32 v18, 4, v18
	v_add3_u32 v26, v160, v18, v159
	s_waitcnt vmcnt(0)
	v_pk_fma_f32 v[14:15], v[14:15], v[250:251], v[204:205]
	v_pk_fma_f32 v[16:17], v[16:17], v[252:253], v[206:207]
	v_pk_fma_f32 v[10:11], v[10:11], v[250:251], v[204:205]
	v_pk_fma_f32 v[12:13], v[12:13], v[252:253], v[206:207]
	v_pk_fma_f32 v[6:7], v[6:7], v[250:251], v[204:205]
	v_pk_fma_f32 v[8:9], v[8:9], v[252:253], v[206:207]
	v_pk_fma_f32 v[2:3], v[2:3], v[250:251], v[204:205]
	v_pk_fma_f32 v[4:5], v[4:5], v[252:253], v[206:207]
	v_cvt_pk_bf16_f32 v14, v14, v15
	v_cvt_pk_bf16_f32 v15, v16, v17
	v_cvt_pk_bf16_f32 v10, v10, v11
	v_cvt_pk_bf16_f32 v11, v12, v13
	v_cvt_pk_bf16_f32 v6, v6, v7
	v_cvt_pk_bf16_f32 v7, v8, v9
	v_add_u32_e32 v8, 0x10000, v26
	v_cvt_pk_bf16_f32 v2, v2, v3
	v_cvt_pk_bf16_f32 v3, v4, v5
	v_add_u32_e32 v4, 0x18000, v26
	ds_write2st64_b64 v26, v[14:15], v[10:11] offset1:64
	ds_write_b64 v8, v[6:7]
	ds_write_b64 v4, v[2:3]
	v_mov_b32_e32 v4, v221
	s_waitcnt lgkmcnt(0)
	s_barrier
	s_load_dwordx2 s[82:83], s[0:1], 0xd8
	s_waitcnt lgkmcnt(0)
	s_add_u32 s4, s82, s4
	v_and_b32_e32 v5, 0x7f, v4
	v_ashrrev_i32_e32 v10, 7, v4
	v_bitop3_b32 v7, v10, v5, 15 bitop3:0x6c
	v_lshlrev_b32_e32 v6, 11, v10
	v_lshlrev_b32_e32 v7, 4, v7
	v_add3_u32 v6, 0, v6, v7
	ds_read_b128 v[6:9], v6
	s_addc_u32 s5, s83, s5
	v_lshlrev_b32_e32 v212, 4, v5
	v_ashrrev_i32_e32 v11, 31, v10
	v_lshl_add_u64 v[2:3], s[4:5], 0, v[212:213]
	v_lshlrev_b64 v[10:11], 11, v[10:11]
	v_lshl_add_u64 v[10:11], v[2:3], 0, v[10:11]
	s_waitcnt lgkmcnt(0)
	global_store_dwordx4 v[10:11], v[6:9], off
	s_lshl_b32 s4, s11, 9
	s_and_b32 s4, s4, 0xffff8000
	v_add_u32_e32 v6, 0x200, v4
	v_ashrrev_i32_e32 v10, 7, v6
	v_bitop3_b32 v7, v10, v5, 15 bitop3:0x6c
	v_lshlrev_b32_e32 v6, 11, v10
	v_lshlrev_b32_e32 v7, 4, v7
	v_add3_u32 v6, 0, v6, v7
	ds_read_b128 v[6:9], v6
	v_ashrrev_i32_e32 v11, 31, v10
	v_lshlrev_b64 v[10:11], 11, v[10:11]
	v_lshl_add_u64 v[10:11], v[2:3], 0, v[10:11]
	s_ashr_i32 s5, s4, 31
	s_waitcnt lgkmcnt(0)
	global_store_dwordx4 v[10:11], v[6:9], off
	s_lshl_b64 s[4:5], s[4:5], 1
	s_add_u32 s4, s18, s4
	v_add_u32_e32 v6, 0x400, v4
	v_ashrrev_i32_e32 v10, 7, v6
	v_bitop3_b32 v7, v10, v5, 15 bitop3:0x6c
	v_lshlrev_b32_e32 v6, 11, v10
	v_lshlrev_b32_e32 v7, 4, v7
	v_add3_u32 v6, 0, v6, v7
	ds_read_b128 v[6:9], v6
	v_ashrrev_i32_e32 v11, 31, v10
	v_lshlrev_b64 v[10:11], 11, v[10:11]
	v_lshl_add_u64 v[10:11], v[2:3], 0, v[10:11]
	s_addc_u32 s5, s19, s5
	s_waitcnt lgkmcnt(0)
	global_store_dwordx4 v[10:11], v[6:9], off
	v_lshlrev_b32_e32 v212, 4, v141
	v_lshl_add_u64 v[98:99], s[4:5], 0, v[212:213]
	v_add_u32_e32 v6, 0x600, v4
	v_ashrrev_i32_e32 v10, 7, v6
	v_bitop3_b32 v7, v10, v5, 15 bitop3:0x6c
	v_lshlrev_b32_e32 v6, 11, v10
	v_lshlrev_b32_e32 v7, 4, v7
	v_add3_u32 v6, 0, v6, v7
	ds_read_b128 v[6:9], v6
	v_ashrrev_i32_e32 v11, 31, v10
	v_lshlrev_b64 v[10:11], 11, v[10:11]
	v_lshl_add_u64 v[10:11], v[2:3], 0, v[10:11]
	v_readlane_b32 s4, v254, 15
	s_waitcnt lgkmcnt(0)
	global_store_dwordx4 v[10:11], v[6:9], off
	s_nop 1
	v_add_u32_e32 v6, 0x800, v4
	v_ashrrev_i32_e32 v10, 7, v6
	v_bitop3_b32 v7, v10, v5, 15 bitop3:0x6c
	v_lshlrev_b32_e32 v6, 11, v10
	v_lshlrev_b32_e32 v7, 4, v7
	v_add3_u32 v6, 0, v6, v7
	ds_read_b128 v[6:9], v6
	v_ashrrev_i32_e32 v11, 31, v10
	v_lshlrev_b64 v[10:11], 11, v[10:11]
	v_lshl_add_u64 v[10:11], v[2:3], 0, v[10:11]
	s_waitcnt lgkmcnt(0)
	global_store_dwordx4 v[10:11], v[6:9], off
	s_nop 1
	v_add_u32_e32 v6, 0xa00, v4
	v_ashrrev_i32_e32 v10, 7, v6
	v_bitop3_b32 v7, v10, v5, 15 bitop3:0x6c
	v_lshlrev_b32_e32 v6, 11, v10
	v_lshlrev_b32_e32 v7, 4, v7
	v_add3_u32 v6, 0, v6, v7
	ds_read_b128 v[6:9], v6
	v_ashrrev_i32_e32 v11, 31, v10
	v_lshlrev_b64 v[10:11], 11, v[10:11]
	v_lshl_add_u64 v[10:11], v[2:3], 0, v[10:11]
	s_waitcnt lgkmcnt(0)
	global_store_dwordx4 v[10:11], v[6:9], off
	s_nop 1
	v_add_u32_e32 v6, 0xc00, v4
	v_ashrrev_i32_e32 v10, 7, v6
	v_bitop3_b32 v7, v10, v5, 15 bitop3:0x6c
	v_lshlrev_b32_e32 v6, 11, v10
	v_lshlrev_b32_e32 v7, 4, v7
	v_add3_u32 v6, 0, v6, v7
	ds_read_b128 v[6:9], v6
	v_ashrrev_i32_e32 v11, 31, v10
	v_lshlrev_b64 v[10:11], 11, v[10:11]
	v_lshl_add_u64 v[10:11], v[2:3], 0, v[10:11]
	s_waitcnt lgkmcnt(0)
	global_store_dwordx4 v[10:11], v[6:9], off
	s_nop 1
	v_add_u32_e32 v6, 0xe00, v4
	v_ashrrev_i32_e32 v10, 7, v6
	v_bitop3_b32 v7, v10, v5, 15 bitop3:0x6c
	v_lshlrev_b32_e32 v6, 11, v10
	v_lshlrev_b32_e32 v7, 4, v7
	v_add3_u32 v6, 0, v6, v7
	ds_read_b128 v[6:9], v6
	v_ashrrev_i32_e32 v11, 31, v10
	v_lshlrev_b64 v[10:11], 11, v[10:11]
	v_lshl_add_u64 v[10:11], v[2:3], 0, v[10:11]
	s_waitcnt lgkmcnt(0)
	global_store_dwordx4 v[10:11], v[6:9], off
	s_nop 1
	v_add_u32_e32 v6, 0x1000, v4
	v_ashrrev_i32_e32 v10, 7, v6
	v_bitop3_b32 v7, v10, v5, 15 bitop3:0x6c
	v_lshlrev_b32_e32 v6, 11, v10
	v_lshlrev_b32_e32 v7, 4, v7
	v_add3_u32 v6, 0, v6, v7
	ds_read_b128 v[6:9], v6
	v_ashrrev_i32_e32 v11, 31, v10
	v_lshlrev_b64 v[10:11], 11, v[10:11]
	v_lshl_add_u64 v[10:11], v[2:3], 0, v[10:11]
	s_waitcnt lgkmcnt(0)
	global_store_dwordx4 v[10:11], v[6:9], off
	s_nop 1
	v_add_u32_e32 v6, 0x1200, v4
	v_ashrrev_i32_e32 v10, 7, v6
	v_bitop3_b32 v7, v10, v5, 15 bitop3:0x6c
	v_lshlrev_b32_e32 v6, 11, v10
	v_lshlrev_b32_e32 v7, 4, v7
	v_add3_u32 v6, 0, v6, v7
	ds_read_b128 v[6:9], v6
	v_ashrrev_i32_e32 v11, 31, v10
	v_lshlrev_b64 v[10:11], 11, v[10:11]
	v_lshl_add_u64 v[10:11], v[2:3], 0, v[10:11]
	s_waitcnt lgkmcnt(0)
	global_store_dwordx4 v[10:11], v[6:9], off
	s_nop 1
	v_add_u32_e32 v6, 0x1400, v4
	v_ashrrev_i32_e32 v10, 7, v6
	v_bitop3_b32 v7, v10, v5, 15 bitop3:0x6c
	v_lshlrev_b32_e32 v6, 11, v10
	v_lshlrev_b32_e32 v7, 4, v7
	v_add3_u32 v6, 0, v6, v7
	ds_read_b128 v[6:9], v6
	v_ashrrev_i32_e32 v11, 31, v10
	v_lshlrev_b64 v[10:11], 11, v[10:11]
	v_lshl_add_u64 v[10:11], v[2:3], 0, v[10:11]
	s_waitcnt lgkmcnt(0)
	global_store_dwordx4 v[10:11], v[6:9], off
	s_nop 1
	v_add_u32_e32 v6, 0x1600, v4
	v_ashrrev_i32_e32 v10, 7, v6
	v_bitop3_b32 v7, v10, v5, 15 bitop3:0x6c
	v_lshlrev_b32_e32 v6, 11, v10
	v_lshlrev_b32_e32 v7, 4, v7
	v_add3_u32 v6, 0, v6, v7
	ds_read_b128 v[6:9], v6
	v_ashrrev_i32_e32 v11, 31, v10
	v_lshlrev_b64 v[10:11], 11, v[10:11]
	v_lshl_add_u64 v[10:11], v[2:3], 0, v[10:11]
	s_waitcnt lgkmcnt(0)
	global_store_dwordx4 v[10:11], v[6:9], off
	s_nop 1
	v_add_u32_e32 v6, 0x1800, v4
	v_ashrrev_i32_e32 v10, 7, v6
	v_bitop3_b32 v7, v10, v5, 15 bitop3:0x6c
	v_lshlrev_b32_e32 v6, 11, v10
	v_lshlrev_b32_e32 v7, 4, v7
	v_add3_u32 v6, 0, v6, v7
	ds_read_b128 v[6:9], v6
	v_ashrrev_i32_e32 v11, 31, v10
	v_lshlrev_b64 v[10:11], 11, v[10:11]
	v_lshl_add_u64 v[10:11], v[2:3], 0, v[10:11]
	s_waitcnt lgkmcnt(0)
	global_store_dwordx4 v[10:11], v[6:9], off
	s_nop 1
	v_add_u32_e32 v6, 0x1a00, v4
	v_ashrrev_i32_e32 v10, 7, v6
	v_bitop3_b32 v7, v10, v5, 15 bitop3:0x6c
	v_lshlrev_b32_e32 v6, 11, v10
	v_lshlrev_b32_e32 v7, 4, v7
	v_add3_u32 v6, 0, v6, v7
	ds_read_b128 v[6:9], v6
	v_ashrrev_i32_e32 v11, 31, v10
	v_lshlrev_b64 v[10:11], 11, v[10:11]
	v_lshl_add_u64 v[10:11], v[2:3], 0, v[10:11]
	s_waitcnt lgkmcnt(0)
	global_store_dwordx4 v[10:11], v[6:9], off
	s_nop 1
	v_add_u32_e32 v6, 0x1c00, v4
	v_ashrrev_i32_e32 v10, 7, v6
	v_bitop3_b32 v7, v10, v5, 15 bitop3:0x6c
	v_lshlrev_b32_e32 v6, 11, v10
	v_lshlrev_b32_e32 v7, 4, v7
	v_add3_u32 v6, 0, v6, v7
	ds_read_b128 v[6:9], v6
	v_ashrrev_i32_e32 v11, 31, v10
	v_lshlrev_b64 v[10:11], 11, v[10:11]
	v_lshl_add_u64 v[10:11], v[2:3], 0, v[10:11]
	v_add_u32_e32 v4, 0x1e00, v4
	s_waitcnt lgkmcnt(0)
	global_store_dwordx4 v[10:11], v[6:9], off
	s_nop 1
	v_ashrrev_i32_e32 v8, 7, v4
	v_bitop3_b32 v5, v8, v5, 15 bitop3:0x6c
	v_lshlrev_b32_e32 v4, 11, v8
	v_lshlrev_b32_e32 v5, 4, v5
	v_add3_u32 v4, 0, v4, v5
	ds_read_b128 v[4:7], v4
	v_ashrrev_i32_e32 v9, 31, v8
	v_lshlrev_b64 v[8:9], 11, v[8:9]
	v_lshl_add_u64 v[2:3], v[2:3], 0, v[8:9]
	s_waitcnt lgkmcnt(0)
	global_store_dwordx4 v[2:3], v[4:7], off
	v_lshl_add_u64 v[2:3], v[98:99], 0, s[22:23]
	global_load_dwordx4 v[34:37], v[2:3], off
	v_add_co_u32_e32 v2, vcc, s72, v2
	s_nop 1
	v_addc_co_u32_e32 v3, vcc, 0, v3, vcc
	global_load_dwordx4 v[42:45], v[2:3], off
	v_lshl_add_u64 v[2:3], v[98:99], 0, s[64:65]
	global_load_dwordx4 v[22:25], v[2:3], off
	v_add_co_u32_e32 v2, vcc, s72, v2
	s_nop 1
	v_addc_co_u32_e32 v3, vcc, 0, v3, vcc
	global_load_dwordx4 v[26:29], v[2:3], off
	v_lshl_add_u64 v[2:3], v[98:99], 0, s[66:67]
	global_load_dwordx4 v[30:33], v[2:3], off
	v_add_co_u32_e32 v2, vcc, s72, v2
	s_nop 1
	v_addc_co_u32_e32 v3, vcc, 0, v3, vcc
	global_load_dwordx4 v[38:41], v[2:3], off
	v_lshl_add_u64 v[2:3], v[98:99], 0, s[68:69]
	global_load_dwordx4 v[46:49], v[2:3], off
	v_add_co_u32_e32 v2, vcc, s72, v2
	s_nop 1
	v_addc_co_u32_e32 v3, vcc, 0, v3, vcc
	global_load_dwordx4 v[50:53], v[2:3], off
	v_bitop3_b32 v2, v100, v145, s4 bitop3:0x36
	v_lshl_add_u32 v2, v2, 4, v160
	ds_read_b128 v[62:65], v2
	ds_read_b128 v[66:69], v2 offset:32768
	v_add_u32_e32 v3, 0x10000, v2
	v_add_u32_e32 v2, 0x18000, v2
	ds_read_b128 v[74:77], v3
	ds_read_b128 v[70:73], v2
	v_mov_b32_e32 v2, 0
	v_readlane_b32 s9, v254, 17
	v_mov_b32_e32 v3, v2
	v_mov_b32_e32 v4, v2
	v_mov_b32_e32 v5, v2
	v_mov_b32_e32 v6, v2
	v_mov_b32_e32 v7, v2
	v_mov_b32_e32 v8, v2
	v_mov_b32_e32 v9, v2
	v_mov_b32_e32 v10, v2
	v_mov_b32_e32 v11, v2
	v_mov_b32_e32 v12, v2
	v_mov_b32_e32 v13, v2
	v_mov_b32_e32 v14, v2
	v_mov_b32_e32 v15, v2
	v_mov_b32_e32 v16, v2
	v_mov_b32_e32 v17, v2
	v_mov_b32_e32 v18, v2
	v_mov_b32_e32 v19, v2
	v_mov_b32_e32 v20, v2
	v_mov_b32_e32 v21, v2
	v_mov_b32_e32 v54, v2
	v_mov_b32_e32 v55, v2
	v_mov_b32_e32 v56, v2
	v_mov_b32_e32 v57, v2
	v_mov_b32_e32 v58, v2
	v_mov_b32_e32 v59, v2
	v_mov_b32_e32 v60, v2
	v_mov_b32_e32 v61, v2
	v_mov_b32_e32 v78, v2
	v_mov_b32_e32 v79, v2
	v_mov_b32_e32 v80, v2
	v_mov_b32_e32 v81, v2
